# v56 + lever 4: one static s_setprio 1 for waves 4-7 through the FoX and NSA attention phases (reset at the output GEMM guard)
# baseline (speedup 1.0000x reference)
; #define PH_END   } if (ph + 1 < hi) { XcdBarrier b2 = bar; b2.bar = (unsigned*)opaque_ptr((unsigned char*)bar.bar); asm volatile("" : "+s"(b2.x)); xcd_barrier(b2); } } ++ph;
; __global__ void __launch_bounds__(NWAVES * 64, 2) fwd_kernel(Args args) {
;     ...
;                 PH_BEGIN_K(7) fox_cum_phase(C, WSP(float, WS_FLOG), args.in[13] + j * 16, WSP(float, WS_CUM)); PH_END
;                 PH_BEGIN_K(7) fox_naive_phase(C, WSP(bf16, WS_R1), WSP(bf16, WS_R1) + (size_t)M * D, WSP(bf16, WS_R1) + (size_t)2 * M * D, WSP(float, WS_CUM), WSP(bf16, WS_O)); PH_END
;     ...
;                 PH_BEGIN_K(7) fox_fast_phase(C, (char*)lds, WSP(bf16, WS_R1), WSP(bf16, WS_R1) + (size_t)M * D, WSP(bf16, WS_R1) + (size_t)2 * M * D, WSP(bf16, WS_O), WSP(float, WS_FLOG), args.in[13] + j * 16, WSP(bf16, WS_Y)); PH_END
.LBB0_877:
	s_andn2_b64 vcc, exec, s[4:5]
	s_cbranch_vccnz .LBB0_1073
	v_readfirstlane_b32 s4, v0
	s_lshr_b32 s4, s4, 8
	s_cmp_lg_u32 s4, 0
	s_cbranch_scc0 .Lprio_skip_fox
	s_setprio 1
.Lprio_skip_fox:
	v_readlane_b32 s4, v253, 32
	v_readlane_b32 s5, v253, 33
	v_readlane_b32 s0, v253, 38
	s_mov_b64 s[8:9], s[4:5]
	v_mov_b32_e32 v226, v0
	v_readlane_b32 s1, v253, 39
	s_load_dword s0, s[0:1], 0x0
	s_mov_b32 s1, s88
	s_waitcnt lgkmcnt(0)
	s_and_b32 s4, s0, 7
	s_cmp_lg_u32 s4, 0
	v_readlane_b32 s6, v253, 34
	v_readlane_b32 s7, v253, 35
	s_cbranch_scc0 .LBB0_880
	s_cmpk_gt_i32 s1, 0xff
	s_cbranch_scc0 .LBB0_881
	s_branch .LBB0_1027

; #define PH_END   } if (ph + 1 < hi) { XcdBarrier b2 = bar; b2.bar = (unsigned*)opaque_ptr((unsigned char*)bar.bar); asm volatile("" : "+s"(b2.x)); xcd_barrier(b2); } } ++ph;
; __global__ void __launch_bounds__(NWAVES * 64, 2) fwd_kernel(Args args) {
;     ...
;                 PH_BEGIN_K(4) { pg8::Gemm g{WSP(bf16, WS_O), WSP(bf16, WS_WFOUT) + (size_t)j * D * D, D, D, D}; pg8::StaticOrder S; S.init(M, D, C.G, C.bx);
;                     pg8::EpiPlain E{WSP(bf16, WS_Y), D}; pg8::gemm_phase<pg8::EpiPlain, pg8::StaticOrder, true, true>(C.lds + RING_OFF, g, S, E); } PH_END
.LBB0_1073:
	s_setprio 0
	v_readlane_b32 s4, v253, 32
	v_readlane_b32 s6, v253, 34
	v_readlane_b32 s5, v253, 33
	v_readlane_b32 s7, v253, 35
	s_cmp_ge_i32 s0, s6
	s_cselect_b64 s[4:5], -1, 0
	s_cmp_lt_i32 s0, s7
	s_cselect_b64 s[0:1], -1, 0
	s_and_b64 s[0:1], s[4:5], s[0:1]
	s_mov_b64 s[4:5], -1
	s_and_b64 vcc, exec, s[0:1]
	s_cbranch_vccnz .LBB0_1075
	v_readlane_b32 s0, v253, 42
	s_add_i32 s0, s0, 6
	s_mov_b64 s[4:5], 0

; #define PH_END   } if (ph + 1 < hi) { XcdBarrier b2 = bar; b2.bar = (unsigned*)opaque_ptr((unsigned char*)bar.bar); asm volatile("" : "+s"(b2.x)); xcd_barrier(b2); } } ++ph;
; __global__ void __launch_bounds__(NWAVES * 64, 2) fwd_kernel(Args args) {
;     ...
;                 PH_BEGIN_K(6) nsa_naive_phase(C, WSP(bf16, WS_R1), WSP(bf16, WS_R1 + R1_KV), WSP(bf16, WS_R1 + R1_KC2), WSP(float, WS_GATES), WSP(float, WS_LUT), WSP(bf16, WS_O)); PH_END
;     ...
;                 PH_BEGIN_K(6) nsa_fast_phase(C, (char*)lds, WSP(bf16, WS_R1), WSP(bf16, WS_R1 + R1_KV), WSP(bf16, WS_R1 + R1_KC2), WSP(float, WS_GATES), WSP(float, WS_LUT), WSP(bf16, WS_O)); PH_END
.LBB0_1361:
	s_andn2_b64 vcc, exec, s[2:3]
	s_cbranch_vccnz .LBB0_1673
	v_readfirstlane_b32 s0, v0
	s_lshr_b32 s0, s0, 8
	s_cmp_lg_u32 s0, 0
	s_cbranch_scc0 .Lprio_skip_nsa
	s_setprio 1
.Lprio_skip_nsa:
	v_readlane_b32 s0, v253, 32
	v_readlane_b32 s1, v253, 33
	v_readlane_b32 s2, v253, 34
	v_readlane_b32 s3, v253, 35
	s_mov_b64 s[2:3], s[0:1]
	v_readlane_b32 s0, v253, 38
	v_mov_b32_e32 v2, v0
	v_readlane_b32 s1, v253, 39
	s_load_dword s0, s[0:1], 0x0
	s_mov_b32 s5, s88
	s_waitcnt lgkmcnt(0)
	s_nop 0
	v_writelane_b32 v252, s0, 2
	s_and_b32 s0, s0, 7
	s_cmp_lg_u32 s0, 0
	s_cbranch_scc0 .LBB0_1364
	s_cmpk_gt_i32 s5, 0xff
	s_cbranch_scc0 .LBB0_1365
	s_branch .LBB0_1627

; #define PH_END   } if (ph + 1 < hi) { XcdBarrier b2 = bar; b2.bar = (unsigned*)opaque_ptr((unsigned char*)bar.bar); asm volatile("" : "+s"(b2.x)); xcd_barrier(b2); } } ++ph;
; __global__ void __launch_bounds__(NWAVES * 64, 2) fwd_kernel(Args args) {
;     ...
;                 PH_BEGIN_K(4) { pg8::Gemm g{WSP(bf16, WS_O), WSP(bf16, WS_WNOUT) + (size_t)j * D * D, D, D, D}; pg8::StaticOrder S; S.init(M, D, C.G, C.bx);
;                     pg8::EpiPlain E{WSP(bf16, WS_Y), D}; pg8::gemm_phase<pg8::EpiPlain, pg8::StaticOrder, true, true>(C.lds + RING_OFF, g, S, E); } PH_END
.LBB0_1673:
	s_setprio 0
	v_readlane_b32 s4, v253, 32
	v_readlane_b32 s6, v253, 34
	v_readlane_b32 s7, v253, 35
	s_cmp_ge_i32 s0, s6
	s_cselect_b64 s[2:3], -1, 0
	s_cmp_lt_i32 s0, s7
	s_cselect_b64 s[0:1], -1, 0
	s_and_b64 s[0:1], s[2:3], s[0:1]
	s_mov_b64 s[2:3], -1
	s_and_b64 vcc, exec, s[0:1]
	v_readlane_b32 s5, v253, 33
	s_cbranch_vccnz .LBB0_1675
	v_readlane_b32 s0, v253, 42
	s_add_i32 s0, s0, 8
	s_mov_b64 s[2:3], 0
